# v109 + first K-loop iteration peeled in the remaining GEMM copies (R1 and both deferred in_proj): every copy except the chain now starts from a zero addend instead of zeroed accumulators
# speedup vs baseline: 1.0072x; 1.0072x over previous
.LBB0_482:
	v_mov_b32_e32 v2, 0
	s_mov_b32 s8, 0
	s_mov_b64 s[36:37], -1
	s_mov_b64 s[58:59], 0
	v_add_u32_e32 v66, 0, v211
	v_add_u32_e32 v132, 0x10000, v66
	v_add_u32_e32 v66, 0x14000, v66
	ds_read_b128 v[148:151], v132
	ds_read_b128 v[152:155], v132 offset:1024
	ds_read_b128 v[156:159], v132 offset:2048
	ds_read_b128 v[160:163], v132 offset:3072
	ds_read_b128 v[132:135], v66
	ds_read_b128 v[136:139], v66 offset:1024
	ds_read_b128 v[140:143], v66 offset:2048
	ds_read_b128 v[144:147], v66 offset:3072
	s_add_u32 s9, s54, s8
	s_addc_u32 s10, s55, 0
	s_and_b64 s[12:13], s[56:57], s[36:37]
	s_xor_b64 s[84:85], s[12:13], -1
	s_add_u32 s12, s9, 0x40080
	s_addc_u32 s13, s10, 0
	v_lshl_add_u64 v[212:213], s[12:13], 0, v[198:199]
	s_add_i32 m0, s91, 0xc000
	ds_read_b128 v[188:191], v228
	ds_read_b128 v[192:195], v228 offset:1024
	ds_read_b128 v[180:183], v228 offset:2048
	ds_read_b128 v[184:187], v228 offset:3072
	ds_read_b128 v[172:175], v228 offset:4096
	ds_read_b128 v[176:179], v228 offset:5120
	ds_read_b128 v[164:167], v228 offset:6144
	ds_read_b128 v[168:171], v228 offset:7168
	global_load_lds_dwordx4 v[212:213], off
	v_lshl_add_u64 v[212:213], s[12:13], 0, v[202:203]
	s_add_i32 m0, s91, 0xe000
	s_and_b64 vcc, exec, s[84:85]
	global_load_lds_dwordx4 v[212:213], off
	s_mov_b64 s[26:27], -1
	s_cbranch_vccz .Lpeelh0_486
	s_waitcnt vmcnt(8)
	s_mov_b64 s[26:27], 0

.Lpeelh0_488:
	s_add_u32 s9, s9, 0x100
	s_addc_u32 s12, s10, 0
	s_and_b64 s[10:11], s[58:59], exec
	s_cselect_b32 s87, s47, s12
	s_cselect_b32 s86, s46, s9
	s_add_u32 s8, s52, s8
	s_addc_u32 s9, s53, 0
	s_add_u32 s10, s8, 0x100
	s_addc_u32 s11, s9, 0
	s_waitcnt lgkmcnt(0)
	s_and_b64 s[8:9], s[58:59], exec
	s_cselect_b32 s59, s49, s11
	s_cselect_b32 s58, s48, s10
	s_barrier
	s_setprio 1
	s_waitcnt lgkmcnt(0)
	v_mfma_f32_16x16x32_bf16 v[128:131], v[148:151], v[188:191], 0
	v_mfma_f32_16x16x32_bf16 v[124:127], v[156:159], v[188:191], 0
	v_mfma_f32_16x16x32_bf16 v[112:115], v[148:151], v[180:183], 0
	v_mfma_f32_16x16x32_bf16 v[108:111], v[156:159], v[180:183], 0
	v_mfma_f32_16x16x32_bf16 v[96:99], v[148:151], v[172:175], 0
	v_mfma_f32_16x16x32_bf16 v[92:95], v[156:159], v[172:175], 0
	v_mfma_f32_16x16x32_bf16 v[80:83], v[148:151], v[164:167], 0
	v_mfma_f32_16x16x32_bf16 v[76:79], v[156:159], v[164:167], 0
	v_mfma_f32_16x16x32_bf16 v[128:131], v[152:155], v[192:195], v[128:131]
	v_mfma_f32_16x16x32_bf16 v[124:127], v[160:163], v[192:195], v[124:127]
	v_mfma_f32_16x16x32_bf16 v[112:115], v[152:155], v[184:187], v[112:115]
	v_mfma_f32_16x16x32_bf16 v[108:111], v[160:163], v[184:187], v[108:111]
	v_mfma_f32_16x16x32_bf16 v[96:99], v[152:155], v[176:179], v[96:99]
	v_mfma_f32_16x16x32_bf16 v[92:95], v[160:163], v[176:179], v[92:95]
	v_mfma_f32_16x16x32_bf16 v[80:83], v[152:155], v[168:171], v[80:83]
	v_mfma_f32_16x16x32_bf16 v[76:79], v[160:163], v[168:171], v[76:79]
	s_setprio 0
	s_setprio 1
	v_mfma_f32_16x16x32_bf16 v[120:123], v[132:135], v[188:191], 0
	v_mfma_f32_16x16x32_bf16 v[116:119], v[140:143], v[188:191], 0
	v_mfma_f32_16x16x32_bf16 v[104:107], v[132:135], v[180:183], 0
	v_mfma_f32_16x16x32_bf16 v[100:103], v[140:143], v[180:183], 0
	v_mfma_f32_16x16x32_bf16 v[88:91], v[132:135], v[172:175], 0
	v_mfma_f32_16x16x32_bf16 v[84:87], v[140:143], v[172:175], 0
	v_mfma_f32_16x16x32_bf16 v[72:75], v[132:135], v[164:167], 0
	v_mfma_f32_16x16x32_bf16 v[68:71], v[140:143], v[164:167], 0
	v_mfma_f32_16x16x32_bf16 v[120:123], v[136:139], v[192:195], v[120:123]
	v_mfma_f32_16x16x32_bf16 v[116:119], v[144:147], v[192:195], v[116:119]
	v_mfma_f32_16x16x32_bf16 v[104:107], v[136:139], v[184:187], v[104:107]
	v_mfma_f32_16x16x32_bf16 v[100:103], v[144:147], v[184:187], v[100:103]
	v_mfma_f32_16x16x32_bf16 v[88:91], v[136:139], v[176:179], v[88:91]
	v_mfma_f32_16x16x32_bf16 v[84:87], v[144:147], v[176:179], v[84:87]
	v_mfma_f32_16x16x32_bf16 v[72:75], v[136:139], v[168:171], v[72:75]
	v_mfma_f32_16x16x32_bf16 v[68:71], v[144:147], v[168:171], v[68:71]
	s_setprio 0
	s_barrier
	s_mov_b32 m0, s92
	v_lshl_add_u64 v[218:219], s[58:59], 0, v[200:201]
	s_add_u32 s8, s58, 0x40000
	ds_read_b128 v[188:191], v228 offset:16384
	ds_read_b128 v[192:195], v228 offset:17408
	ds_read_b128 v[180:183], v228 offset:18432
	ds_read_b128 v[184:187], v228 offset:19456
	ds_read_b128 v[172:175], v228 offset:20480
	ds_read_b128 v[176:179], v228 offset:21504
	ds_read_b128 v[164:167], v228 offset:22528
	ds_read_b128 v[168:171], v228 offset:23552
	global_load_lds_dwordx4 v[218:219], off
	v_lshl_add_u64 v[216:217], s[58:59], 0, v[208:209]
	s_mov_b32 m0, s93
	s_addc_u32 s9, s59, 0
	global_load_lds_dwordx4 v[216:217], off
	v_lshl_add_u64 v[212:213], s[8:9], 0, v[200:201]
	s_mov_b32 m0, s94
	v_lshl_add_u64 v[214:215], s[86:87], 0, v[202:203]
	global_load_lds_dwordx4 v[212:213], off
	v_lshl_add_u64 v[212:213], s[8:9], 0, v[208:209]
	s_mov_b32 m0, s95
	s_mov_b64 s[26:27], -1
	global_load_lds_dwordx4 v[212:213], off
	v_lshl_add_u64 v[212:213], s[86:87], 0, v[198:199]
	s_mov_b32 m0, s91
	s_and_b64 vcc, exec, s[84:85]
	global_load_lds_dwordx4 v[212:213], off
	s_mov_b32 m0, s96
	s_nop 0
	global_load_lds_dwordx4 v[214:215], off
	s_cbranch_vccz .Lpeelh0_490
	s_waitcnt vmcnt(8)
	s_mov_b64 s[26:27], 0

.Lpeelh0_T:
	s_waitcnt lgkmcnt(0)
	s_xor_b64 s[84:85], s[36:37], -1
	s_barrier
	s_setprio 1
	s_waitcnt lgkmcnt(0)
	v_mfma_f32_16x16x32_bf16 v[62:65], v[148:151], v[188:191], 0
	v_mfma_f32_16x16x32_bf16 v[58:61], v[156:159], v[188:191], 0
	v_mfma_f32_16x16x32_bf16 v[46:49], v[148:151], v[180:183], 0
	v_mfma_f32_16x16x32_bf16 v[42:45], v[156:159], v[180:183], 0
	v_mfma_f32_16x16x32_bf16 v[30:33], v[148:151], v[172:175], 0
	v_mfma_f32_16x16x32_bf16 v[26:29], v[156:159], v[172:175], 0
	v_mfma_f32_16x16x32_bf16 v[14:17], v[148:151], v[164:167], 0
	v_mfma_f32_16x16x32_bf16 v[10:13], v[156:159], v[164:167], 0
	v_mfma_f32_16x16x32_bf16 v[62:65], v[152:155], v[192:195], v[62:65]
	v_mfma_f32_16x16x32_bf16 v[58:61], v[160:163], v[192:195], v[58:61]
	v_mfma_f32_16x16x32_bf16 v[46:49], v[152:155], v[184:187], v[46:49]
	v_mfma_f32_16x16x32_bf16 v[42:45], v[160:163], v[184:187], v[42:45]
	v_mfma_f32_16x16x32_bf16 v[30:33], v[152:155], v[176:179], v[30:33]
	v_mfma_f32_16x16x32_bf16 v[26:29], v[160:163], v[176:179], v[26:29]
	v_mfma_f32_16x16x32_bf16 v[14:17], v[152:155], v[168:171], v[14:17]
	v_mfma_f32_16x16x32_bf16 v[10:13], v[160:163], v[168:171], v[10:13]
	s_setprio 0
	s_setprio 1
	v_mfma_f32_16x16x32_bf16 v[54:57], v[132:135], v[188:191], 0
	v_mfma_f32_16x16x32_bf16 v[50:53], v[140:143], v[188:191], 0
	v_mfma_f32_16x16x32_bf16 v[38:41], v[132:135], v[180:183], 0
	v_mfma_f32_16x16x32_bf16 v[34:37], v[140:143], v[180:183], 0
	v_mfma_f32_16x16x32_bf16 v[22:25], v[132:135], v[172:175], 0
	v_mfma_f32_16x16x32_bf16 v[18:21], v[140:143], v[172:175], 0
	v_mfma_f32_16x16x32_bf16 v[6:9], v[132:135], v[164:167], 0
	v_mfma_f32_16x16x32_bf16 v[2:5], v[140:143], v[164:167], 0
	v_mfma_f32_16x16x32_bf16 v[54:57], v[136:139], v[192:195], v[54:57]
	v_mfma_f32_16x16x32_bf16 v[50:53], v[144:147], v[192:195], v[50:53]
	v_mfma_f32_16x16x32_bf16 v[38:41], v[136:139], v[184:187], v[38:41]
	v_mfma_f32_16x16x32_bf16 v[34:37], v[144:147], v[184:187], v[34:37]
	v_mfma_f32_16x16x32_bf16 v[22:25], v[136:139], v[176:179], v[22:25]
	v_mfma_f32_16x16x32_bf16 v[18:21], v[144:147], v[176:179], v[18:21]
	v_mfma_f32_16x16x32_bf16 v[6:9], v[136:139], v[168:171], v[6:9]
	v_mfma_f32_16x16x32_bf16 v[2:5], v[144:147], v[168:171], v[2:5]
	s_setprio 0
	s_barrier
	s_add_i32 s10, 0, 0x18000
	v_add_u32_e32 v66, s10, v211
	s_add_i32 s11, 0, 0x1c000
	ds_read_b128 v[132:135], v66
	ds_read_b128 v[136:139], v66 offset:1024
	ds_read_b128 v[140:143], v66 offset:2048
	ds_read_b128 v[144:147], v66 offset:3072
	v_add_u32_e32 v66, s11, v211
	ds_read_b128 v[148:151], v66
	ds_read_b128 v[152:155], v66 offset:1024
	ds_read_b128 v[156:159], v66 offset:2048
	ds_read_b128 v[160:163], v66 offset:3072
	s_add_u32 s8, s86, 0x40000
	s_addc_u32 s9, s87, 0
	s_mov_b32 m0, s97
	v_lshl_add_u64 v[230:231], s[8:9], 0, v[198:199]
	ds_read_b128 v[164:167], v228 offset:32768
	ds_read_b128 v[168:171], v228 offset:33792
	ds_read_b128 v[172:175], v228 offset:34816
	ds_read_b128 v[176:179], v228 offset:35840
	ds_read_b128 v[180:183], v228 offset:36864
	ds_read_b128 v[184:187], v228 offset:37888
	ds_read_b128 v[188:191], v228 offset:38912
	ds_read_b128 v[192:195], v228 offset:39936
	global_load_lds_dwordx4 v[230:231], off
	v_lshl_add_u64 v[230:231], s[8:9], 0, v[202:203]
	s_mov_b32 m0, s64
	s_nop 0
	global_load_lds_dwordx4 v[230:231], off
	s_waitcnt vmcnt(8)
	s_waitcnt lgkmcnt(0)
	s_barrier
	s_setprio 1
	s_waitcnt lgkmcnt(0)
	v_mfma_f32_16x16x32_bf16 v[128:131], v[132:135], v[164:167], v[128:131]
	v_mfma_f32_16x16x32_bf16 v[124:127], v[140:143], v[164:167], v[124:127]
	v_mfma_f32_16x16x32_bf16 v[112:115], v[132:135], v[172:175], v[112:115]
	v_mfma_f32_16x16x32_bf16 v[108:111], v[140:143], v[172:175], v[108:111]
	v_mfma_f32_16x16x32_bf16 v[96:99], v[132:135], v[180:183], v[96:99]
	v_mfma_f32_16x16x32_bf16 v[92:95], v[140:143], v[180:183], v[92:95]
	v_mfma_f32_16x16x32_bf16 v[80:83], v[132:135], v[188:191], v[80:83]
	v_mfma_f32_16x16x32_bf16 v[76:79], v[140:143], v[188:191], v[76:79]
	v_mfma_f32_16x16x32_bf16 v[128:131], v[136:139], v[168:171], v[128:131]
	v_mfma_f32_16x16x32_bf16 v[124:127], v[144:147], v[168:171], v[124:127]
	v_mfma_f32_16x16x32_bf16 v[112:115], v[136:139], v[176:179], v[112:115]
	v_mfma_f32_16x16x32_bf16 v[108:111], v[144:147], v[176:179], v[108:111]
	v_mfma_f32_16x16x32_bf16 v[96:99], v[136:139], v[184:187], v[96:99]
	v_mfma_f32_16x16x32_bf16 v[92:95], v[144:147], v[184:187], v[92:95]
	v_mfma_f32_16x16x32_bf16 v[80:83], v[136:139], v[192:195], v[80:83]
	v_mfma_f32_16x16x32_bf16 v[76:79], v[144:147], v[192:195], v[76:79]
	s_setprio 0
	s_setprio 1
	v_mfma_f32_16x16x32_bf16 v[120:123], v[148:151], v[164:167], v[120:123]
	v_mfma_f32_16x16x32_bf16 v[116:119], v[156:159], v[164:167], v[116:119]
	v_mfma_f32_16x16x32_bf16 v[104:107], v[148:151], v[172:175], v[104:107]
	v_mfma_f32_16x16x32_bf16 v[100:103], v[156:159], v[172:175], v[100:103]
	v_mfma_f32_16x16x32_bf16 v[88:91], v[148:151], v[180:183], v[88:91]
	v_mfma_f32_16x16x32_bf16 v[84:87], v[156:159], v[180:183], v[84:87]
	v_mfma_f32_16x16x32_bf16 v[72:75], v[148:151], v[188:191], v[72:75]
	v_mfma_f32_16x16x32_bf16 v[68:71], v[156:159], v[188:191], v[68:71]
	v_mfma_f32_16x16x32_bf16 v[120:123], v[152:155], v[168:171], v[120:123]
	v_mfma_f32_16x16x32_bf16 v[116:119], v[160:163], v[168:171], v[116:119]
	v_mfma_f32_16x16x32_bf16 v[104:107], v[152:155], v[176:179], v[104:107]
	v_mfma_f32_16x16x32_bf16 v[100:103], v[160:163], v[176:179], v[100:103]
	v_mfma_f32_16x16x32_bf16 v[88:91], v[152:155], v[184:187], v[88:91]
	v_mfma_f32_16x16x32_bf16 v[84:87], v[160:163], v[184:187], v[84:87]
	v_mfma_f32_16x16x32_bf16 v[72:75], v[152:155], v[192:195], v[72:75]
	v_mfma_f32_16x16x32_bf16 v[68:71], v[160:163], v[192:195], v[68:71]
	s_setprio 0
	s_barrier
	s_add_i32 s8, s10, s90
	v_lshl_add_u64 v[218:219], v[218:219], 0, s[60:61]
	s_mov_b32 m0, s8
	ds_read_b128 v[164:167], v228 offset:49152
	ds_read_b128 v[168:171], v228 offset:50176
	ds_read_b128 v[172:175], v228 offset:51200
	ds_read_b128 v[176:179], v228 offset:52224
	ds_read_b128 v[180:183], v228 offset:53248
	ds_read_b128 v[184:187], v228 offset:54272
	ds_read_b128 v[188:191], v228 offset:55296
	ds_read_b128 v[192:195], v228 offset:56320
	global_load_lds_dwordx4 v[218:219], off
	s_add_i32 m0, s8, 0x2000
	s_add_u32 s8, s58, 0x40080
	v_lshl_add_u64 v[216:217], v[216:217], 0, s[60:61]
	s_addc_u32 s9, s59, 0
	s_add_i32 s10, s11, s90
	global_load_lds_dwordx4 v[216:217], off
	v_lshl_add_u64 v[216:217], s[8:9], 0, v[200:201]
	s_mov_b32 m0, s10
	v_lshl_add_u64 v[212:213], v[212:213], 0, s[60:61]
	global_load_lds_dwordx4 v[216:217], off
	v_lshl_add_u64 v[216:217], s[8:9], 0, v[208:209]
	s_add_i32 m0, s10, 0x2000
	s_nop 0
	global_load_lds_dwordx4 v[216:217], off
	s_mov_b32 m0, s65
	s_nop 0
	global_load_lds_dwordx4 v[212:213], off
	v_lshl_add_u64 v[212:213], v[214:215], 0, s[60:61]
	s_mov_b32 m0, s68
	s_nop 0
	global_load_lds_dwordx4 v[212:213], off
	s_waitcnt vmcnt(8)
	s_waitcnt lgkmcnt(0)
	s_barrier
	s_setprio 1
	s_waitcnt lgkmcnt(0)
	v_mfma_f32_16x16x32_bf16 v[62:65], v[132:135], v[164:167], v[62:65]
	v_mfma_f32_16x16x32_bf16 v[58:61], v[140:143], v[164:167], v[58:61]
	v_mfma_f32_16x16x32_bf16 v[46:49], v[132:135], v[172:175], v[46:49]
	v_mfma_f32_16x16x32_bf16 v[42:45], v[140:143], v[172:175], v[42:45]
	v_mfma_f32_16x16x32_bf16 v[30:33], v[132:135], v[180:183], v[30:33]
	v_mfma_f32_16x16x32_bf16 v[26:29], v[140:143], v[180:183], v[26:29]
	v_mfma_f32_16x16x32_bf16 v[14:17], v[132:135], v[188:191], v[14:17]
	v_mfma_f32_16x16x32_bf16 v[10:13], v[140:143], v[188:191], v[10:13]
	v_mfma_f32_16x16x32_bf16 v[62:65], v[136:139], v[168:171], v[62:65]
	v_mfma_f32_16x16x32_bf16 v[58:61], v[144:147], v[168:171], v[58:61]
	v_mfma_f32_16x16x32_bf16 v[46:49], v[136:139], v[176:179], v[46:49]
	v_mfma_f32_16x16x32_bf16 v[42:45], v[144:147], v[176:179], v[42:45]
	v_mfma_f32_16x16x32_bf16 v[30:33], v[136:139], v[184:187], v[30:33]
	v_mfma_f32_16x16x32_bf16 v[26:29], v[144:147], v[184:187], v[26:29]
	v_mfma_f32_16x16x32_bf16 v[14:17], v[136:139], v[192:195], v[14:17]
	v_mfma_f32_16x16x32_bf16 v[10:13], v[144:147], v[192:195], v[10:13]
	s_setprio 0
	s_setprio 1
	v_mfma_f32_16x16x32_bf16 v[54:57], v[148:151], v[164:167], v[54:57]
	v_mfma_f32_16x16x32_bf16 v[50:53], v[156:159], v[164:167], v[50:53]
	v_mfma_f32_16x16x32_bf16 v[38:41], v[148:151], v[172:175], v[38:41]
	v_mfma_f32_16x16x32_bf16 v[34:37], v[156:159], v[172:175], v[34:37]
	v_mfma_f32_16x16x32_bf16 v[22:25], v[148:151], v[180:183], v[22:25]
	v_mfma_f32_16x16x32_bf16 v[18:21], v[156:159], v[180:183], v[18:21]
	v_mfma_f32_16x16x32_bf16 v[6:9], v[148:151], v[188:191], v[6:9]
	v_mfma_f32_16x16x32_bf16 v[2:5], v[156:159], v[188:191], v[2:5]
	v_mfma_f32_16x16x32_bf16 v[54:57], v[152:155], v[168:171], v[54:57]
	v_mfma_f32_16x16x32_bf16 v[50:53], v[160:163], v[168:171], v[50:53]
	v_mfma_f32_16x16x32_bf16 v[38:41], v[152:155], v[176:179], v[38:41]
	v_mfma_f32_16x16x32_bf16 v[34:37], v[160:163], v[176:179], v[34:37]
	v_mfma_f32_16x16x32_bf16 v[22:25], v[152:155], v[184:187], v[22:25]
	v_mfma_f32_16x16x32_bf16 v[18:21], v[160:163], v[184:187], v[18:21]
	v_mfma_f32_16x16x32_bf16 v[6:9], v[152:155], v[192:195], v[6:9]
	v_mfma_f32_16x16x32_bf16 v[2:5], v[160:163], v[192:195], v[2:5]
	s_setprio 0
	s_barrier
	s_movk_i32 s8, 0x100
	s_mov_b64 s[36:37], 0
	s_mov_b64 s[58:59], -1
	s_and_b64 vcc, exec, s[84:85]
	s_cbranch_vccnz .LBB0_492
	s_branch .LBB0_484

.LBB0_506:
	s_add_u32 s8, s46, 0x40080
	s_addc_u32 s9, s47, 0
	s_add_u32 s89, s36, 0x100
	v_mov_b32_e32 v2, 0
	v_lshl_add_u64 v[212:213], s[8:9], 0, v[208:209]
	v_lshl_add_u64 v[214:215], s[8:9], 0, v[210:211]
	s_addc_u32 s90, s37, 0
	s_mov_b32 s91, -2
	s_mov_b64 s[48:49], 0
	s_xor_b64 s[50:51], s[50:51], -1
	v_add_u32_e32 v132, 0, v205
	v_add_u32_e32 v133, 0x10000, v132
	v_add_u32_e32 v144, 0x14000, v132
	ds_read_b128 v[148:151], v133
	ds_read_b128 v[152:155], v133 offset:1024
	ds_read_b128 v[156:159], v133 offset:2048
	ds_read_b128 v[160:163], v133 offset:3072
	ds_read_b128 v[132:135], v144
	ds_read_b128 v[136:139], v144 offset:1024
	ds_read_b128 v[140:143], v144 offset:2048
	ds_read_b128 v[144:147], v144 offset:3072
	s_cmp_lg_u32 s48, 0
	s_cselect_b64 s[8:9], -1, 0
	s_mov_b64 s[26:27], -1
	s_or_b64 s[54:55], s[50:51], s[8:9]
	v_lshl_add_u64 v[216:217], v[212:213], 0, s[48:49]
	s_add_i32 m0, s58, 0xc000
	ds_read_b128 v[188:191], v226
	ds_read_b128 v[192:195], v226 offset:1024
	ds_read_b128 v[180:183], v226 offset:2048
	ds_read_b128 v[184:187], v226 offset:3072
	ds_read_b128 v[172:175], v226 offset:4096
	ds_read_b128 v[176:179], v226 offset:5120
	ds_read_b128 v[164:167], v226 offset:6144
	ds_read_b128 v[168:171], v226 offset:7168
	global_load_lds_dwordx4 v[216:217], off
	v_lshl_add_u64 v[216:217], v[214:215], 0, s[48:49]
	s_add_i32 m0, s58, 0xe000
	s_and_b64 vcc, exec, s[54:55]
	global_load_lds_dwordx4 v[216:217], off
	s_cbranch_vccz .Lpeelh1_510
	s_waitcnt vmcnt(8)
	s_mov_b64 s[26:27], 0

.Lpeelh1_512:
	s_add_u32 s8, s46, s48
	s_addc_u32 s9, s47, s49
	s_add_u32 s8, s8, 0x100
	s_addc_u32 s9, s9, 0
	s_add_u32 s10, s89, s48
	s_addc_u32 s11, s90, s49
	s_waitcnt lgkmcnt(0)
	s_cmpk_eq_i32 s48, 0x700
	s_cselect_b32 s53, s41, s9
	s_cselect_b32 s52, s40, s8
	s_cselect_b32 s37, s43, s11
	s_cselect_b32 s36, s42, s10
	s_barrier
	s_setprio 1
	s_waitcnt lgkmcnt(0)
	v_mfma_f32_16x16x32_bf16 v[128:131], v[148:151], v[188:191], 0
	v_mfma_f32_16x16x32_bf16 v[124:127], v[156:159], v[188:191], 0
	v_mfma_f32_16x16x32_bf16 v[120:123], v[148:151], v[180:183], 0
	v_mfma_f32_16x16x32_bf16 v[112:115], v[156:159], v[180:183], 0
	v_mfma_f32_16x16x32_bf16 v[104:107], v[148:151], v[172:175], 0
	v_mfma_f32_16x16x32_bf16 v[96:99], v[156:159], v[172:175], 0
	v_mfma_f32_16x16x32_bf16 v[88:91], v[148:151], v[164:167], 0
	v_mfma_f32_16x16x32_bf16 v[80:83], v[156:159], v[164:167], 0
	v_mfma_f32_16x16x32_bf16 v[128:131], v[152:155], v[192:195], v[128:131]
	v_mfma_f32_16x16x32_bf16 v[124:127], v[160:163], v[192:195], v[124:127]
	v_mfma_f32_16x16x32_bf16 v[120:123], v[152:155], v[184:187], v[120:123]
	v_mfma_f32_16x16x32_bf16 v[112:115], v[160:163], v[184:187], v[112:115]
	v_mfma_f32_16x16x32_bf16 v[104:107], v[152:155], v[176:179], v[104:107]
	v_mfma_f32_16x16x32_bf16 v[96:99], v[160:163], v[176:179], v[96:99]
	v_mfma_f32_16x16x32_bf16 v[88:91], v[152:155], v[168:171], v[88:91]
	v_mfma_f32_16x16x32_bf16 v[80:83], v[160:163], v[168:171], v[80:83]
	s_setprio 0
	s_setprio 1
	v_mfma_f32_16x16x32_bf16 v[116:119], v[132:135], v[188:191], 0
	v_mfma_f32_16x16x32_bf16 v[108:111], v[140:143], v[188:191], 0
	v_mfma_f32_16x16x32_bf16 v[100:103], v[132:135], v[180:183], 0
	v_mfma_f32_16x16x32_bf16 v[92:95], v[140:143], v[180:183], 0
	v_mfma_f32_16x16x32_bf16 v[84:87], v[132:135], v[172:175], 0
	v_mfma_f32_16x16x32_bf16 v[76:79], v[140:143], v[172:175], 0
	v_mfma_f32_16x16x32_bf16 v[72:75], v[132:135], v[164:167], 0
	v_mfma_f32_16x16x32_bf16 v[68:71], v[140:143], v[164:167], 0
	v_mfma_f32_16x16x32_bf16 v[116:119], v[136:139], v[192:195], v[116:119]
	v_mfma_f32_16x16x32_bf16 v[108:111], v[144:147], v[192:195], v[108:111]
	v_mfma_f32_16x16x32_bf16 v[100:103], v[136:139], v[184:187], v[100:103]
	v_mfma_f32_16x16x32_bf16 v[92:95], v[144:147], v[184:187], v[92:95]
	v_mfma_f32_16x16x32_bf16 v[84:87], v[136:139], v[176:179], v[84:87]
	v_mfma_f32_16x16x32_bf16 v[76:79], v[144:147], v[176:179], v[76:79]
	v_mfma_f32_16x16x32_bf16 v[72:75], v[136:139], v[168:171], v[72:75]
	v_mfma_f32_16x16x32_bf16 v[68:71], v[144:147], v[168:171], v[68:71]
	s_setprio 0
	s_barrier
	s_mov_b32 m0, s59
	v_lshl_add_u64 v[222:223], s[36:37], 0, v[198:199]
	s_add_u32 s8, s36, 0x40000
	ds_read_b128 v[188:191], v226 offset:16384
	ds_read_b128 v[192:195], v226 offset:17408
	ds_read_b128 v[180:183], v226 offset:18432
	ds_read_b128 v[184:187], v226 offset:19456
	ds_read_b128 v[172:175], v226 offset:20480
	ds_read_b128 v[176:179], v226 offset:21504
	ds_read_b128 v[164:167], v226 offset:22528
	ds_read_b128 v[168:171], v226 offset:23552
	global_load_lds_dwordx4 v[222:223], off
	v_lshl_add_u64 v[220:221], s[36:37], 0, v[202:203]
	s_mov_b32 m0, s64
	s_addc_u32 s9, s37, 0
	global_load_lds_dwordx4 v[220:221], off
	v_lshl_add_u64 v[216:217], s[8:9], 0, v[198:199]
	s_mov_b32 m0, s65
	v_lshl_add_u64 v[218:219], s[52:53], 0, v[200:201]
	global_load_lds_dwordx4 v[216:217], off
	v_lshl_add_u64 v[216:217], s[8:9], 0, v[202:203]
	s_mov_b32 m0, s68
	s_mov_b64 s[26:27], -1
	global_load_lds_dwordx4 v[216:217], off
	v_lshl_add_u64 v[216:217], s[52:53], 0, v[66:67]
	s_mov_b32 m0, s58
	s_and_b64 vcc, exec, s[54:55]
	global_load_lds_dwordx4 v[216:217], off
	s_mov_b32 m0, s69
	s_nop 0
	global_load_lds_dwordx4 v[218:219], off
	s_cbranch_vccz .Lpeelh1_514
	s_waitcnt vmcnt(8)
	s_mov_b64 s[26:27], 0

.Lpeelh1_T:
	s_waitcnt lgkmcnt(0)
	s_barrier
	s_setprio 1
	s_waitcnt lgkmcnt(0)
	v_mfma_f32_16x16x32_bf16 v[62:65], v[148:151], v[188:191], 0
	v_mfma_f32_16x16x32_bf16 v[58:61], v[156:159], v[188:191], 0
	v_mfma_f32_16x16x32_bf16 v[54:57], v[148:151], v[180:183], 0
	v_mfma_f32_16x16x32_bf16 v[46:49], v[156:159], v[180:183], 0
	v_mfma_f32_16x16x32_bf16 v[38:41], v[148:151], v[172:175], 0
	v_mfma_f32_16x16x32_bf16 v[30:33], v[156:159], v[172:175], 0
	v_mfma_f32_16x16x32_bf16 v[22:25], v[148:151], v[164:167], 0
	v_mfma_f32_16x16x32_bf16 v[14:17], v[156:159], v[164:167], 0
	v_mfma_f32_16x16x32_bf16 v[62:65], v[152:155], v[192:195], v[62:65]
	v_mfma_f32_16x16x32_bf16 v[58:61], v[160:163], v[192:195], v[58:61]
	v_mfma_f32_16x16x32_bf16 v[54:57], v[152:155], v[184:187], v[54:57]
	v_mfma_f32_16x16x32_bf16 v[46:49], v[160:163], v[184:187], v[46:49]
	v_mfma_f32_16x16x32_bf16 v[38:41], v[152:155], v[176:179], v[38:41]
	v_mfma_f32_16x16x32_bf16 v[30:33], v[160:163], v[176:179], v[30:33]
	v_mfma_f32_16x16x32_bf16 v[22:25], v[152:155], v[168:171], v[22:25]
	v_mfma_f32_16x16x32_bf16 v[14:17], v[160:163], v[168:171], v[14:17]
	s_setprio 0
	s_setprio 1
	v_mfma_f32_16x16x32_bf16 v[50:53], v[132:135], v[188:191], 0
	v_mfma_f32_16x16x32_bf16 v[42:45], v[140:143], v[188:191], 0
	v_mfma_f32_16x16x32_bf16 v[34:37], v[132:135], v[180:183], 0
	v_mfma_f32_16x16x32_bf16 v[26:29], v[140:143], v[180:183], 0
	v_mfma_f32_16x16x32_bf16 v[18:21], v[132:135], v[172:175], 0
	v_mfma_f32_16x16x32_bf16 v[10:13], v[140:143], v[172:175], 0
	v_mfma_f32_16x16x32_bf16 v[6:9], v[132:135], v[164:167], 0
	v_mfma_f32_16x16x32_bf16 v[2:5], v[140:143], v[164:167], 0
	v_mfma_f32_16x16x32_bf16 v[50:53], v[136:139], v[192:195], v[50:53]
	v_mfma_f32_16x16x32_bf16 v[42:45], v[144:147], v[192:195], v[42:45]
	v_mfma_f32_16x16x32_bf16 v[34:37], v[136:139], v[184:187], v[34:37]
	v_mfma_f32_16x16x32_bf16 v[26:29], v[144:147], v[184:187], v[26:29]
	v_mfma_f32_16x16x32_bf16 v[18:21], v[136:139], v[176:179], v[18:21]
	v_mfma_f32_16x16x32_bf16 v[10:13], v[144:147], v[176:179], v[10:13]
	v_mfma_f32_16x16x32_bf16 v[6:9], v[136:139], v[168:171], v[6:9]
	v_mfma_f32_16x16x32_bf16 v[2:5], v[144:147], v[168:171], v[2:5]
	s_setprio 0
	s_barrier
	s_add_i32 s10, 0, 0x18000
	s_add_i32 s11, 0, 0x1c000
	v_add_u32_e32 v144, s10, v205
	v_add_u32_e32 v160, s11, v205
	ds_read_b128 v[132:135], v144
	ds_read_b128 v[136:139], v144 offset:1024
	ds_read_b128 v[140:143], v144 offset:2048
	ds_read_b128 v[144:147], v144 offset:3072
	ds_read_b128 v[148:151], v160
	ds_read_b128 v[152:155], v160 offset:1024
	ds_read_b128 v[156:159], v160 offset:2048
	ds_read_b128 v[160:163], v160 offset:3072
	s_add_u32 s8, s52, 0x40000
	s_addc_u32 s9, s53, 0
	s_mov_b32 m0, s70
	v_lshl_add_u64 v[228:229], s[8:9], 0, v[66:67]
	ds_read_b128 v[164:167], v226 offset:32768
	ds_read_b128 v[168:171], v226 offset:33792
	ds_read_b128 v[172:175], v226 offset:34816
	ds_read_b128 v[176:179], v226 offset:35840
	ds_read_b128 v[180:183], v226 offset:36864
	ds_read_b128 v[184:187], v226 offset:37888
	ds_read_b128 v[188:191], v226 offset:38912
	ds_read_b128 v[192:195], v226 offset:39936
	global_load_lds_dwordx4 v[228:229], off
	v_lshl_add_u64 v[228:229], s[8:9], 0, v[200:201]
	s_mov_b32 m0, s71
	s_nop 0
	global_load_lds_dwordx4 v[228:229], off
	s_waitcnt vmcnt(8)
	s_waitcnt lgkmcnt(0)
	s_barrier
	s_setprio 1
	s_waitcnt lgkmcnt(0)
	v_mfma_f32_16x16x32_bf16 v[128:131], v[132:135], v[164:167], v[128:131]
	v_mfma_f32_16x16x32_bf16 v[124:127], v[140:143], v[164:167], v[124:127]
	v_mfma_f32_16x16x32_bf16 v[120:123], v[132:135], v[172:175], v[120:123]
	v_mfma_f32_16x16x32_bf16 v[112:115], v[140:143], v[172:175], v[112:115]
	v_mfma_f32_16x16x32_bf16 v[104:107], v[132:135], v[180:183], v[104:107]
	v_mfma_f32_16x16x32_bf16 v[96:99], v[140:143], v[180:183], v[96:99]
	v_mfma_f32_16x16x32_bf16 v[88:91], v[132:135], v[188:191], v[88:91]
	v_mfma_f32_16x16x32_bf16 v[80:83], v[140:143], v[188:191], v[80:83]
	v_mfma_f32_16x16x32_bf16 v[128:131], v[136:139], v[168:171], v[128:131]
	v_mfma_f32_16x16x32_bf16 v[124:127], v[144:147], v[168:171], v[124:127]
	v_mfma_f32_16x16x32_bf16 v[120:123], v[136:139], v[176:179], v[120:123]
	v_mfma_f32_16x16x32_bf16 v[112:115], v[144:147], v[176:179], v[112:115]
	v_mfma_f32_16x16x32_bf16 v[104:107], v[136:139], v[184:187], v[104:107]
	v_mfma_f32_16x16x32_bf16 v[96:99], v[144:147], v[184:187], v[96:99]
	v_mfma_f32_16x16x32_bf16 v[88:91], v[136:139], v[192:195], v[88:91]
	v_mfma_f32_16x16x32_bf16 v[80:83], v[144:147], v[192:195], v[80:83]
	s_setprio 0
	s_setprio 1
	v_mfma_f32_16x16x32_bf16 v[116:119], v[148:151], v[164:167], v[116:119]
	v_mfma_f32_16x16x32_bf16 v[108:111], v[156:159], v[164:167], v[108:111]
	v_mfma_f32_16x16x32_bf16 v[100:103], v[148:151], v[172:175], v[100:103]
	v_mfma_f32_16x16x32_bf16 v[92:95], v[156:159], v[172:175], v[92:95]
	v_mfma_f32_16x16x32_bf16 v[84:87], v[148:151], v[180:183], v[84:87]
	v_mfma_f32_16x16x32_bf16 v[76:79], v[156:159], v[180:183], v[76:79]
	v_mfma_f32_16x16x32_bf16 v[72:75], v[148:151], v[188:191], v[72:75]
	v_mfma_f32_16x16x32_bf16 v[68:71], v[156:159], v[188:191], v[68:71]
	v_mfma_f32_16x16x32_bf16 v[116:119], v[152:155], v[168:171], v[116:119]
	v_mfma_f32_16x16x32_bf16 v[108:111], v[160:163], v[168:171], v[108:111]
	v_mfma_f32_16x16x32_bf16 v[100:103], v[152:155], v[176:179], v[100:103]
	v_mfma_f32_16x16x32_bf16 v[92:95], v[160:163], v[176:179], v[92:95]
	v_mfma_f32_16x16x32_bf16 v[84:87], v[152:155], v[184:187], v[84:87]
	v_mfma_f32_16x16x32_bf16 v[76:79], v[160:163], v[184:187], v[76:79]
	v_mfma_f32_16x16x32_bf16 v[72:75], v[152:155], v[192:195], v[72:75]
	v_mfma_f32_16x16x32_bf16 v[68:71], v[160:163], v[192:195], v[68:71]
	s_setprio 0
	s_barrier
	s_add_i32 s8, s10, s57
	v_lshl_add_u64 v[222:223], v[222:223], 0, s[60:61]
	s_mov_b32 m0, s8
	ds_read_b128 v[164:167], v226 offset:49152
	ds_read_b128 v[168:171], v226 offset:50176
	ds_read_b128 v[172:175], v226 offset:51200
	ds_read_b128 v[176:179], v226 offset:52224
	ds_read_b128 v[180:183], v226 offset:53248
	ds_read_b128 v[184:187], v226 offset:54272
	ds_read_b128 v[188:191], v226 offset:55296
	ds_read_b128 v[192:195], v226 offset:56320
	global_load_lds_dwordx4 v[222:223], off
	s_add_i32 m0, s8, 0x2000
	s_add_u32 s8, s36, 0x40080
	v_lshl_add_u64 v[220:221], v[220:221], 0, s[60:61]
	s_addc_u32 s9, s37, 0
	s_add_i32 s10, s11, s57
	global_load_lds_dwordx4 v[220:221], off
	v_lshl_add_u64 v[220:221], s[8:9], 0, v[198:199]
	s_mov_b32 m0, s10
	v_lshl_add_u64 v[216:217], v[216:217], 0, s[60:61]
	global_load_lds_dwordx4 v[220:221], off
	v_lshl_add_u64 v[220:221], s[8:9], 0, v[202:203]
	s_add_i32 m0, s10, 0x2000
	s_nop 0
	global_load_lds_dwordx4 v[220:221], off
	s_mov_b32 m0, s72
	s_nop 0
	global_load_lds_dwordx4 v[216:217], off
	v_lshl_add_u64 v[216:217], v[218:219], 0, s[60:61]
	s_mov_b32 m0, s84
	s_nop 0
	global_load_lds_dwordx4 v[216:217], off
	s_waitcnt vmcnt(8)
	s_waitcnt lgkmcnt(0)
	s_barrier
	s_setprio 1
	s_waitcnt lgkmcnt(0)
	v_mfma_f32_16x16x32_bf16 v[62:65], v[132:135], v[164:167], v[62:65]
	v_mfma_f32_16x16x32_bf16 v[58:61], v[140:143], v[164:167], v[58:61]
	v_mfma_f32_16x16x32_bf16 v[54:57], v[132:135], v[172:175], v[54:57]
	v_mfma_f32_16x16x32_bf16 v[46:49], v[140:143], v[172:175], v[46:49]
	v_mfma_f32_16x16x32_bf16 v[38:41], v[132:135], v[180:183], v[38:41]
	v_mfma_f32_16x16x32_bf16 v[30:33], v[140:143], v[180:183], v[30:33]
	v_mfma_f32_16x16x32_bf16 v[22:25], v[132:135], v[188:191], v[22:25]
	v_mfma_f32_16x16x32_bf16 v[14:17], v[140:143], v[188:191], v[14:17]
	v_mfma_f32_16x16x32_bf16 v[62:65], v[136:139], v[168:171], v[62:65]
	v_mfma_f32_16x16x32_bf16 v[58:61], v[144:147], v[168:171], v[58:61]
	v_mfma_f32_16x16x32_bf16 v[54:57], v[136:139], v[176:179], v[54:57]
	v_mfma_f32_16x16x32_bf16 v[46:49], v[144:147], v[176:179], v[46:49]
	v_mfma_f32_16x16x32_bf16 v[38:41], v[136:139], v[184:187], v[38:41]
	v_mfma_f32_16x16x32_bf16 v[30:33], v[144:147], v[184:187], v[30:33]
	v_mfma_f32_16x16x32_bf16 v[22:25], v[136:139], v[192:195], v[22:25]
	v_mfma_f32_16x16x32_bf16 v[14:17], v[144:147], v[192:195], v[14:17]
	s_setprio 0
	s_setprio 1
	v_mfma_f32_16x16x32_bf16 v[50:53], v[148:151], v[164:167], v[50:53]
	v_mfma_f32_16x16x32_bf16 v[42:45], v[156:159], v[164:167], v[42:45]
	v_mfma_f32_16x16x32_bf16 v[34:37], v[148:151], v[172:175], v[34:37]
	v_mfma_f32_16x16x32_bf16 v[26:29], v[156:159], v[172:175], v[26:29]
	v_mfma_f32_16x16x32_bf16 v[18:21], v[148:151], v[180:183], v[18:21]
	v_mfma_f32_16x16x32_bf16 v[10:13], v[156:159], v[180:183], v[10:13]
	v_mfma_f32_16x16x32_bf16 v[6:9], v[148:151], v[188:191], v[6:9]
	v_mfma_f32_16x16x32_bf16 v[2:5], v[156:159], v[188:191], v[2:5]
	v_mfma_f32_16x16x32_bf16 v[50:53], v[152:155], v[168:171], v[50:53]
	v_mfma_f32_16x16x32_bf16 v[42:45], v[160:163], v[168:171], v[42:45]
	v_mfma_f32_16x16x32_bf16 v[34:37], v[152:155], v[176:179], v[34:37]
	v_mfma_f32_16x16x32_bf16 v[26:29], v[160:163], v[176:179], v[26:29]
	v_mfma_f32_16x16x32_bf16 v[18:21], v[152:155], v[184:187], v[18:21]
	v_mfma_f32_16x16x32_bf16 v[10:13], v[160:163], v[184:187], v[10:13]
	v_mfma_f32_16x16x32_bf16 v[6:9], v[152:155], v[192:195], v[6:9]
	v_mfma_f32_16x16x32_bf16 v[2:5], v[160:163], v[192:195], v[2:5]
	s_setprio 0
	s_barrier
	s_add_i32 s91, s91, 2
	s_add_u32 s48, s48, 0x100
	s_addc_u32 s49, s49, 0
	s_cmp_gt_u32 s91, 13
	s_cbranch_scc1 .LBB0_516
	s_branch .LBB0_508

.LBB0_677:
	s_add_u32 s8, s46, 0x40080
	s_addc_u32 s9, s47, 0
	s_add_u32 s89, s36, 0x100
	v_mov_b32_e32 v2, 0
	v_lshl_add_u64 v[210:211], s[8:9], 0, v[202:203]
	v_lshl_add_u64 v[212:213], s[8:9], 0, v[208:209]
	s_addc_u32 s90, s37, 0
	s_mov_b32 s91, -2
	s_mov_b64 s[48:49], 0
	s_xor_b64 s[50:51], s[50:51], -1
	v_add_u32_e32 v132, 0, v222
	v_add_u32_e32 v133, 0x10000, v132
	v_add_u32_e32 v144, 0x14000, v132
	ds_read_b128 v[148:151], v133
	ds_read_b128 v[152:155], v133 offset:1024
	ds_read_b128 v[156:159], v133 offset:2048
	ds_read_b128 v[160:163], v133 offset:3072
	ds_read_b128 v[132:135], v144
	ds_read_b128 v[136:139], v144 offset:1024
	ds_read_b128 v[140:143], v144 offset:2048
	ds_read_b128 v[144:147], v144 offset:3072
	s_cmp_lg_u32 s48, 0
	s_cselect_b64 s[8:9], -1, 0
	s_mov_b64 s[26:27], -1
	s_or_b64 s[54:55], s[50:51], s[8:9]
	v_lshl_add_u64 v[214:215], v[210:211], 0, s[48:49]
	s_add_i32 m0, s58, 0xc000
	ds_read_b128 v[188:191], v224
	ds_read_b128 v[192:195], v224 offset:1024
	ds_read_b128 v[180:183], v224 offset:2048
	ds_read_b128 v[184:187], v224 offset:3072
	ds_read_b128 v[172:175], v224 offset:4096
	ds_read_b128 v[176:179], v224 offset:5120
	ds_read_b128 v[164:167], v224 offset:6144
	ds_read_b128 v[168:171], v224 offset:7168
	global_load_lds_dwordx4 v[214:215], off
	v_lshl_add_u64 v[214:215], v[212:213], 0, s[48:49]
	s_add_i32 m0, s58, 0xe000
	s_and_b64 vcc, exec, s[54:55]
	global_load_lds_dwordx4 v[214:215], off
	s_cbranch_vccz .Lpeelh2_681
	s_waitcnt vmcnt(8)
	s_mov_b64 s[26:27], 0

.Lpeelh2_683:
	s_add_u32 s8, s46, s48
	s_addc_u32 s9, s47, s49
	s_add_u32 s8, s8, 0x100
	s_addc_u32 s9, s9, 0
	s_add_u32 s10, s89, s48
	s_addc_u32 s11, s90, s49
	s_waitcnt lgkmcnt(0)
	s_cmpk_eq_i32 s48, 0x700
	s_cselect_b32 s53, s41, s9
	s_cselect_b32 s52, s40, s8
	s_cselect_b32 s37, s43, s11
	s_cselect_b32 s36, s42, s10
	s_barrier
	s_setprio 1
	s_waitcnt lgkmcnt(0)
	v_mfma_f32_16x16x32_bf16 v[128:131], v[148:151], v[188:191], 0
	v_mfma_f32_16x16x32_bf16 v[124:127], v[156:159], v[188:191], 0
	v_mfma_f32_16x16x32_bf16 v[120:123], v[148:151], v[180:183], 0
	v_mfma_f32_16x16x32_bf16 v[112:115], v[156:159], v[180:183], 0
	v_mfma_f32_16x16x32_bf16 v[104:107], v[148:151], v[172:175], 0
	v_mfma_f32_16x16x32_bf16 v[96:99], v[156:159], v[172:175], 0
	v_mfma_f32_16x16x32_bf16 v[88:91], v[148:151], v[164:167], 0
	v_mfma_f32_16x16x32_bf16 v[80:83], v[156:159], v[164:167], 0
	v_mfma_f32_16x16x32_bf16 v[128:131], v[152:155], v[192:195], v[128:131]
	v_mfma_f32_16x16x32_bf16 v[124:127], v[160:163], v[192:195], v[124:127]
	v_mfma_f32_16x16x32_bf16 v[120:123], v[152:155], v[184:187], v[120:123]
	v_mfma_f32_16x16x32_bf16 v[112:115], v[160:163], v[184:187], v[112:115]
	v_mfma_f32_16x16x32_bf16 v[104:107], v[152:155], v[176:179], v[104:107]
	v_mfma_f32_16x16x32_bf16 v[96:99], v[160:163], v[176:179], v[96:99]
	v_mfma_f32_16x16x32_bf16 v[88:91], v[152:155], v[168:171], v[88:91]
	v_mfma_f32_16x16x32_bf16 v[80:83], v[160:163], v[168:171], v[80:83]
	s_setprio 0
	s_setprio 1
	v_mfma_f32_16x16x32_bf16 v[116:119], v[132:135], v[188:191], 0
	v_mfma_f32_16x16x32_bf16 v[108:111], v[140:143], v[188:191], 0
	v_mfma_f32_16x16x32_bf16 v[100:103], v[132:135], v[180:183], 0
	v_mfma_f32_16x16x32_bf16 v[92:95], v[140:143], v[180:183], 0
	v_mfma_f32_16x16x32_bf16 v[84:87], v[132:135], v[172:175], 0
	v_mfma_f32_16x16x32_bf16 v[76:79], v[140:143], v[172:175], 0
	v_mfma_f32_16x16x32_bf16 v[72:75], v[132:135], v[164:167], 0
	v_mfma_f32_16x16x32_bf16 v[68:71], v[140:143], v[164:167], 0
	v_mfma_f32_16x16x32_bf16 v[116:119], v[136:139], v[192:195], v[116:119]
	v_mfma_f32_16x16x32_bf16 v[108:111], v[144:147], v[192:195], v[108:111]
	v_mfma_f32_16x16x32_bf16 v[100:103], v[136:139], v[184:187], v[100:103]
	v_mfma_f32_16x16x32_bf16 v[92:95], v[144:147], v[184:187], v[92:95]
	v_mfma_f32_16x16x32_bf16 v[84:87], v[136:139], v[176:179], v[84:87]
	v_mfma_f32_16x16x32_bf16 v[76:79], v[144:147], v[176:179], v[76:79]
	v_mfma_f32_16x16x32_bf16 v[72:75], v[136:139], v[168:171], v[72:75]
	v_mfma_f32_16x16x32_bf16 v[68:71], v[144:147], v[168:171], v[68:71]
	s_setprio 0
	s_barrier
	s_mov_b32 m0, s59
	v_lshl_add_u64 v[220:221], s[36:37], 0, v[196:197]
	s_add_u32 s8, s36, 0x40000
	ds_read_b128 v[188:191], v224 offset:16384
	ds_read_b128 v[192:195], v224 offset:17408
	ds_read_b128 v[180:183], v224 offset:18432
	ds_read_b128 v[184:187], v224 offset:19456
	ds_read_b128 v[172:175], v224 offset:20480
	ds_read_b128 v[176:179], v224 offset:21504
	ds_read_b128 v[164:167], v224 offset:22528
	ds_read_b128 v[168:171], v224 offset:23552
	global_load_lds_dwordx4 v[220:221], off
	v_lshl_add_u64 v[218:219], s[36:37], 0, v[200:201]
	s_mov_b32 m0, s64
	s_addc_u32 s9, s37, 0
	global_load_lds_dwordx4 v[218:219], off
	v_lshl_add_u64 v[214:215], s[8:9], 0, v[196:197]
	s_mov_b32 m0, s65
	v_lshl_add_u64 v[216:217], s[52:53], 0, v[198:199]
	global_load_lds_dwordx4 v[214:215], off
	v_lshl_add_u64 v[214:215], s[8:9], 0, v[200:201]
	s_mov_b32 m0, s68
	s_mov_b64 s[26:27], -1
	global_load_lds_dwordx4 v[214:215], off
	v_lshl_add_u64 v[214:215], s[52:53], 0, v[66:67]
	s_mov_b32 m0, s58
	s_and_b64 vcc, exec, s[54:55]
	global_load_lds_dwordx4 v[214:215], off
	s_mov_b32 m0, s69
	s_nop 0
	global_load_lds_dwordx4 v[216:217], off
	s_cbranch_vccz .Lpeelh2_685
	s_waitcnt vmcnt(8)
	s_mov_b64 s[26:27], 0

.Lpeelh2_T:
	s_waitcnt lgkmcnt(0)
	s_barrier
	s_setprio 1
	s_waitcnt lgkmcnt(0)
	v_mfma_f32_16x16x32_bf16 v[62:65], v[148:151], v[188:191], 0
	v_mfma_f32_16x16x32_bf16 v[58:61], v[156:159], v[188:191], 0
	v_mfma_f32_16x16x32_bf16 v[54:57], v[148:151], v[180:183], 0
	v_mfma_f32_16x16x32_bf16 v[46:49], v[156:159], v[180:183], 0
	v_mfma_f32_16x16x32_bf16 v[38:41], v[148:151], v[172:175], 0
	v_mfma_f32_16x16x32_bf16 v[30:33], v[156:159], v[172:175], 0
	v_mfma_f32_16x16x32_bf16 v[22:25], v[148:151], v[164:167], 0
	v_mfma_f32_16x16x32_bf16 v[14:17], v[156:159], v[164:167], 0
	v_mfma_f32_16x16x32_bf16 v[62:65], v[152:155], v[192:195], v[62:65]
	v_mfma_f32_16x16x32_bf16 v[58:61], v[160:163], v[192:195], v[58:61]
	v_mfma_f32_16x16x32_bf16 v[54:57], v[152:155], v[184:187], v[54:57]
	v_mfma_f32_16x16x32_bf16 v[46:49], v[160:163], v[184:187], v[46:49]
	v_mfma_f32_16x16x32_bf16 v[38:41], v[152:155], v[176:179], v[38:41]
	v_mfma_f32_16x16x32_bf16 v[30:33], v[160:163], v[176:179], v[30:33]
	v_mfma_f32_16x16x32_bf16 v[22:25], v[152:155], v[168:171], v[22:25]
	v_mfma_f32_16x16x32_bf16 v[14:17], v[160:163], v[168:171], v[14:17]
	s_setprio 0
	s_setprio 1
	v_mfma_f32_16x16x32_bf16 v[50:53], v[132:135], v[188:191], 0
	v_mfma_f32_16x16x32_bf16 v[42:45], v[140:143], v[188:191], 0
	v_mfma_f32_16x16x32_bf16 v[34:37], v[132:135], v[180:183], 0
	v_mfma_f32_16x16x32_bf16 v[26:29], v[140:143], v[180:183], 0
	v_mfma_f32_16x16x32_bf16 v[18:21], v[132:135], v[172:175], 0
	v_mfma_f32_16x16x32_bf16 v[10:13], v[140:143], v[172:175], 0
	v_mfma_f32_16x16x32_bf16 v[6:9], v[132:135], v[164:167], 0
	v_mfma_f32_16x16x32_bf16 v[2:5], v[140:143], v[164:167], 0
	v_mfma_f32_16x16x32_bf16 v[50:53], v[136:139], v[192:195], v[50:53]
	v_mfma_f32_16x16x32_bf16 v[42:45], v[144:147], v[192:195], v[42:45]
	v_mfma_f32_16x16x32_bf16 v[34:37], v[136:139], v[184:187], v[34:37]
	v_mfma_f32_16x16x32_bf16 v[26:29], v[144:147], v[184:187], v[26:29]
	v_mfma_f32_16x16x32_bf16 v[18:21], v[136:139], v[176:179], v[18:21]
	v_mfma_f32_16x16x32_bf16 v[10:13], v[144:147], v[176:179], v[10:13]
	v_mfma_f32_16x16x32_bf16 v[6:9], v[136:139], v[168:171], v[6:9]
	v_mfma_f32_16x16x32_bf16 v[2:5], v[144:147], v[168:171], v[2:5]
	s_setprio 0
	s_barrier
	s_add_i32 s10, 0, 0x18000
	s_add_i32 s11, 0, 0x1c000
	v_add_u32_e32 v144, s10, v222
	v_add_u32_e32 v160, s11, v222
	ds_read_b128 v[132:135], v144
	ds_read_b128 v[136:139], v144 offset:1024
	ds_read_b128 v[140:143], v144 offset:2048
	ds_read_b128 v[144:147], v144 offset:3072
	ds_read_b128 v[148:151], v160
	ds_read_b128 v[152:155], v160 offset:1024
	ds_read_b128 v[156:159], v160 offset:2048
	ds_read_b128 v[160:163], v160 offset:3072
	s_add_u32 s8, s52, 0x40000
	s_addc_u32 s9, s53, 0
	s_mov_b32 m0, s70
	v_lshl_add_u64 v[226:227], s[8:9], 0, v[66:67]
	ds_read_b128 v[164:167], v224 offset:32768
	ds_read_b128 v[168:171], v224 offset:33792
	ds_read_b128 v[172:175], v224 offset:34816
	ds_read_b128 v[176:179], v224 offset:35840
	ds_read_b128 v[180:183], v224 offset:36864
	ds_read_b128 v[184:187], v224 offset:37888
	ds_read_b128 v[188:191], v224 offset:38912
	ds_read_b128 v[192:195], v224 offset:39936
	global_load_lds_dwordx4 v[226:227], off
	v_lshl_add_u64 v[226:227], s[8:9], 0, v[198:199]
	s_mov_b32 m0, s71
	s_nop 0
	global_load_lds_dwordx4 v[226:227], off
	s_waitcnt vmcnt(8)
	s_waitcnt lgkmcnt(0)
	s_barrier
	s_setprio 1
	s_waitcnt lgkmcnt(0)
	v_mfma_f32_16x16x32_bf16 v[128:131], v[132:135], v[164:167], v[128:131]
	v_mfma_f32_16x16x32_bf16 v[124:127], v[140:143], v[164:167], v[124:127]
	v_mfma_f32_16x16x32_bf16 v[120:123], v[132:135], v[172:175], v[120:123]
	v_mfma_f32_16x16x32_bf16 v[112:115], v[140:143], v[172:175], v[112:115]
	v_mfma_f32_16x16x32_bf16 v[104:107], v[132:135], v[180:183], v[104:107]
	v_mfma_f32_16x16x32_bf16 v[96:99], v[140:143], v[180:183], v[96:99]
	v_mfma_f32_16x16x32_bf16 v[88:91], v[132:135], v[188:191], v[88:91]
	v_mfma_f32_16x16x32_bf16 v[80:83], v[140:143], v[188:191], v[80:83]
	v_mfma_f32_16x16x32_bf16 v[128:131], v[136:139], v[168:171], v[128:131]
	v_mfma_f32_16x16x32_bf16 v[124:127], v[144:147], v[168:171], v[124:127]
	v_mfma_f32_16x16x32_bf16 v[120:123], v[136:139], v[176:179], v[120:123]
	v_mfma_f32_16x16x32_bf16 v[112:115], v[144:147], v[176:179], v[112:115]
	v_mfma_f32_16x16x32_bf16 v[104:107], v[136:139], v[184:187], v[104:107]
	v_mfma_f32_16x16x32_bf16 v[96:99], v[144:147], v[184:187], v[96:99]
	v_mfma_f32_16x16x32_bf16 v[88:91], v[136:139], v[192:195], v[88:91]
	v_mfma_f32_16x16x32_bf16 v[80:83], v[144:147], v[192:195], v[80:83]
	s_setprio 0
	s_setprio 1
	v_mfma_f32_16x16x32_bf16 v[116:119], v[148:151], v[164:167], v[116:119]
	v_mfma_f32_16x16x32_bf16 v[108:111], v[156:159], v[164:167], v[108:111]
	v_mfma_f32_16x16x32_bf16 v[100:103], v[148:151], v[172:175], v[100:103]
	v_mfma_f32_16x16x32_bf16 v[92:95], v[156:159], v[172:175], v[92:95]
	v_mfma_f32_16x16x32_bf16 v[84:87], v[148:151], v[180:183], v[84:87]
	v_mfma_f32_16x16x32_bf16 v[76:79], v[156:159], v[180:183], v[76:79]
	v_mfma_f32_16x16x32_bf16 v[72:75], v[148:151], v[188:191], v[72:75]
	v_mfma_f32_16x16x32_bf16 v[68:71], v[156:159], v[188:191], v[68:71]
	v_mfma_f32_16x16x32_bf16 v[116:119], v[152:155], v[168:171], v[116:119]
	v_mfma_f32_16x16x32_bf16 v[108:111], v[160:163], v[168:171], v[108:111]
	v_mfma_f32_16x16x32_bf16 v[100:103], v[152:155], v[176:179], v[100:103]
	v_mfma_f32_16x16x32_bf16 v[92:95], v[160:163], v[176:179], v[92:95]
	v_mfma_f32_16x16x32_bf16 v[84:87], v[152:155], v[184:187], v[84:87]
	v_mfma_f32_16x16x32_bf16 v[76:79], v[160:163], v[184:187], v[76:79]
	v_mfma_f32_16x16x32_bf16 v[72:75], v[152:155], v[192:195], v[72:75]
	v_mfma_f32_16x16x32_bf16 v[68:71], v[160:163], v[192:195], v[68:71]
	s_setprio 0
	s_barrier
	s_add_i32 s8, s10, s57
	v_lshl_add_u64 v[220:221], v[220:221], 0, s[60:61]
	s_mov_b32 m0, s8
	ds_read_b128 v[164:167], v224 offset:49152
	ds_read_b128 v[168:171], v224 offset:50176
	ds_read_b128 v[172:175], v224 offset:51200
	ds_read_b128 v[176:179], v224 offset:52224
	ds_read_b128 v[180:183], v224 offset:53248
	ds_read_b128 v[184:187], v224 offset:54272
	ds_read_b128 v[188:191], v224 offset:55296
	ds_read_b128 v[192:195], v224 offset:56320
	global_load_lds_dwordx4 v[220:221], off
	s_add_i32 m0, s8, 0x2000
	s_add_u32 s8, s36, 0x40080
	v_lshl_add_u64 v[218:219], v[218:219], 0, s[60:61]
	s_addc_u32 s9, s37, 0
	s_add_i32 s10, s11, s57
	global_load_lds_dwordx4 v[218:219], off
	v_lshl_add_u64 v[218:219], s[8:9], 0, v[196:197]
	s_mov_b32 m0, s10
	v_lshl_add_u64 v[214:215], v[214:215], 0, s[60:61]
	global_load_lds_dwordx4 v[218:219], off
	v_lshl_add_u64 v[218:219], s[8:9], 0, v[200:201]
	s_add_i32 m0, s10, 0x2000
	s_nop 0
	global_load_lds_dwordx4 v[218:219], off
	s_mov_b32 m0, s72
	s_nop 0
	global_load_lds_dwordx4 v[214:215], off
	v_lshl_add_u64 v[214:215], v[216:217], 0, s[60:61]
	s_mov_b32 m0, s84
	s_nop 0
	global_load_lds_dwordx4 v[214:215], off
	s_waitcnt vmcnt(8)
	s_waitcnt lgkmcnt(0)
	s_barrier
	s_setprio 1
	s_waitcnt lgkmcnt(0)
	v_mfma_f32_16x16x32_bf16 v[62:65], v[132:135], v[164:167], v[62:65]
	v_mfma_f32_16x16x32_bf16 v[58:61], v[140:143], v[164:167], v[58:61]
	v_mfma_f32_16x16x32_bf16 v[54:57], v[132:135], v[172:175], v[54:57]
	v_mfma_f32_16x16x32_bf16 v[46:49], v[140:143], v[172:175], v[46:49]
	v_mfma_f32_16x16x32_bf16 v[38:41], v[132:135], v[180:183], v[38:41]
	v_mfma_f32_16x16x32_bf16 v[30:33], v[140:143], v[180:183], v[30:33]
	v_mfma_f32_16x16x32_bf16 v[22:25], v[132:135], v[188:191], v[22:25]
	v_mfma_f32_16x16x32_bf16 v[14:17], v[140:143], v[188:191], v[14:17]
	v_mfma_f32_16x16x32_bf16 v[62:65], v[136:139], v[168:171], v[62:65]
	v_mfma_f32_16x16x32_bf16 v[58:61], v[144:147], v[168:171], v[58:61]
	v_mfma_f32_16x16x32_bf16 v[54:57], v[136:139], v[176:179], v[54:57]
	v_mfma_f32_16x16x32_bf16 v[46:49], v[144:147], v[176:179], v[46:49]
	v_mfma_f32_16x16x32_bf16 v[38:41], v[136:139], v[184:187], v[38:41]
	v_mfma_f32_16x16x32_bf16 v[30:33], v[144:147], v[184:187], v[30:33]
	v_mfma_f32_16x16x32_bf16 v[22:25], v[136:139], v[192:195], v[22:25]
	v_mfma_f32_16x16x32_bf16 v[14:17], v[144:147], v[192:195], v[14:17]
	s_setprio 0
	s_setprio 1
	v_mfma_f32_16x16x32_bf16 v[50:53], v[148:151], v[164:167], v[50:53]
	v_mfma_f32_16x16x32_bf16 v[42:45], v[156:159], v[164:167], v[42:45]
	v_mfma_f32_16x16x32_bf16 v[34:37], v[148:151], v[172:175], v[34:37]
	v_mfma_f32_16x16x32_bf16 v[26:29], v[156:159], v[172:175], v[26:29]
	v_mfma_f32_16x16x32_bf16 v[18:21], v[148:151], v[180:183], v[18:21]
	v_mfma_f32_16x16x32_bf16 v[10:13], v[156:159], v[180:183], v[10:13]
	v_mfma_f32_16x16x32_bf16 v[6:9], v[148:151], v[188:191], v[6:9]
	v_mfma_f32_16x16x32_bf16 v[2:5], v[156:159], v[188:191], v[2:5]
	v_mfma_f32_16x16x32_bf16 v[50:53], v[152:155], v[168:171], v[50:53]
	v_mfma_f32_16x16x32_bf16 v[42:45], v[160:163], v[168:171], v[42:45]
	v_mfma_f32_16x16x32_bf16 v[34:37], v[152:155], v[176:179], v[34:37]
	v_mfma_f32_16x16x32_bf16 v[26:29], v[160:163], v[176:179], v[26:29]
	v_mfma_f32_16x16x32_bf16 v[18:21], v[152:155], v[184:187], v[18:21]
	v_mfma_f32_16x16x32_bf16 v[10:13], v[160:163], v[184:187], v[10:13]
	v_mfma_f32_16x16x32_bf16 v[6:9], v[152:155], v[192:195], v[6:9]
	v_mfma_f32_16x16x32_bf16 v[2:5], v[160:163], v[192:195], v[2:5]
	s_setprio 0
	s_barrier
	s_add_i32 s91, s91, 2
	s_add_u32 s48, s48, 0x100
	s_addc_u32 s49, s49, 0
	s_cmp_gt_u32 s91, 13
	s_cbranch_scc1 .LBB0_687
	s_branch .LBB0_679
